# baseline (speedup 1.0000x reference)
.Lpro_wc_done:
	s_lshr_b32 s0, s33, 8
	s_lshl_b32 s1, s37, 4
	v_and_or_b32 v104, s1, 48, v82
	s_waitcnt lgkmcnt(0)
	v_mov_b32_e32 v62, 0x15300
	v_lshl_or_b32 v62, v104, 2, v62
	v_lshlrev_b32_e32 v109, 5, v106
	s_barrier
	ds_read_b32 v105, v62
	v_or_b32_e32 v62, 0x15000, v109
	v_or_b32_e32 v84, 0x15100, v109
	ds_read_b128 v[62:65], v62
	ds_read_b128 v[84:87], v84
	s_lshl_b32 s1, s0, 6
	s_add_i32 s2, s1, 0x14c00
	v_lshlrev_b32_e32 v108, 4, v106
	v_or_b32_e32 v88, s2, v108
	s_waitcnt lgkmcnt(0)
	v_fma_f32 v63, v105, v63, v85
	v_lshlrev_b32_e32 v92, 4, v1
	v_max_f32_e32 v101, 0, v63
	v_or_b32_e32 v63, 0x15010, v109
	ds_read_b128 v[88:91], v88 offset:1536
	v_lshl_or_b32 v100, s0, 11, v92
	v_fma_f32 v62, v105, v62, v84
	v_or_b32_e32 v84, 0x15110, v109
	ds_read_b128 v[92:95], v63
	ds_read_b128 v[96:99], v84
	v_fmac_f32_e32 v87, v105, v65
	v_fma_f32 v63, v105, v64, v86
	v_max_f32_e32 v102, 0, v87
	v_max_f32_e32 v62, 0, v62
	s_waitcnt lgkmcnt(0)
	v_fma_f32 v65, v105, v93, v97
	v_fma_f32 v64, v105, v92, v96
	v_max_f32_e32 v92, 0, v65
	v_fma_f32 v65, v105, v94, v98
	v_fmac_f32_e32 v99, v105, v95
	v_max_f32_e32 v65, 0, v65
	v_max_f32_e32 v84, 0, v99
	v_cvt_pk_f16_f32 v65, v65, v84
	ds_read_b128 v[84:87], v100 offset:36864
	v_max_f32_e32 v64, 0, v64
	v_cvt_pk_f16_f32 v64, v64, v92
	v_or_b32_e32 v92, 0x15080, v109
	v_or_b32_e32 v96, 0x15180, v109
	ds_read_b128 v[92:95], v92
	ds_read_b128 v[96:99], v96
	v_max_f32_e32 v63, 0, v63
	v_cvt_pk_f16_f32 v63, v63, v102
	v_cvt_pk_f16_f32 v62, v62, v101
	ds_read_b128 v[100:103], v100 offset:37888
	s_waitcnt lgkmcnt(1)
	v_fma_f32 v94, v105, v94, v98
	v_mfma_f32_16x16x32_f16 v[62:65], v[84:87], v[62:65], v[88:91]
	v_fma_f32 v84, v105, v92, v96
	v_max_f32_e32 v92, 0, v84
	v_fma_f32 v84, v105, v93, v97
	v_max_f32_e32 v93, 0, v84
	v_or_b32_e32 v84, 0x15090, v109
	v_or_b32_e32 v88, 0x15190, v109
	ds_read_b128 v[84:87], v84
	ds_read_b128 v[88:91], v88
	v_fmac_f32_e32 v99, v105, v95
	v_max_f32_e32 v94, 0, v94
	v_max_f32_e32 v95, 0, v99
	s_add_i32 s1, s1, 0xb000
	s_waitcnt lgkmcnt(0)
	v_fma_f32 v84, v105, v84, v88
	v_fma_f32 v85, v105, v85, v89
	v_fma_f32 v86, v105, v86, v90
	v_fmac_f32_e32 v91, v105, v87
	v_max_f32_e32 v84, 0, v84
	v_max_f32_e32 v85, 0, v85
	v_max_f32_e32 v86, 0, v86
	v_max_f32_e32 v87, 0, v91
	v_cvt_pk_f16_f32 v87, v86, v87
	v_cvt_pk_f16_f32 v86, v84, v85
	v_cvt_pk_f16_f32 v85, v94, v95
	v_cvt_pk_f16_f32 v84, v92, v93
	v_cmp_eq_u32_e64 s[12:13], 1, v106
	v_cmp_eq_u32_e64 s[2:3], 0, v1
	v_mfma_f32_16x16x32_f16 v[62:65], v[100:103], v[84:87], v[62:65]
	v_mul_u32_u24_e32 v84, 0x110, v104
	v_add3_u32 v84, s1, v84, v108
	v_or_b32_e32 v112, 4, v106
	v_or_b32_e32 v116, 60, v106
	s_nop 3
	ds_write_b128 v84, v[62:65]
	v_mbcnt_lo_u32_b32 v62, -1, 0
	v_mbcnt_hi_u32_b32 v62, -1, v62
	v_and_or_b32 v62, v62, 64, v82
	v_lshlrev_b32_e32 v108, 2, v62
	v_mov_b32_e32 v62, 0x13c00
	v_lshl_or_b32 v111, v106, 2, v62
	v_mov_b32_e32 v62, 0xf400
	v_lshl_or_b32 v113, v83, 2, v62
	v_and_b32_e32 v62, 8, v0
	v_cmp_eq_u32_e64 s[4:5], 0, v62
	v_and_b32_e32 v62, 4, v0
	v_cmp_eq_u32_e64 s[6:7], 0, v62
	v_and_b32_e32 v62, 2, v0
	v_and_b32_e32 v0, 1, v0
	v_cmp_eq_u32_e64 s[10:11], 0, v0
	v_mov_b32_e32 v0, 0x13400
	v_cmp_eq_u32_e64 s[8:9], 0, v62
	v_lshl_or_b32 v117, v1, 1, v0
	v_mov_b32_e32 v0, s14
	v_mov_b32_e32 v62, s26
	v_cndmask_b32_e64 v0, v0, v62, s[12:13]
	v_mov_b32_e32 v62, s15
	v_mov_b32_e32 v63, s27
	v_cndmask_b32_e64 v62, v62, v63, s[12:13]
	v_mov_b32_e32 v63, s25
	v_cmp_gt_u32_e64 s[14:15], 16, v1
	v_or_b32_e32 v109, 64, v108
	v_or_b32_e32 v110, 0x80, v108
	v_cndmask_b32_e64 v1, v62, v63, s[14:15]
	v_mov_b32_e32 v62, s24
	v_cndmask_b32_e64 v0, v0, v62, s[14:15]
	v_mov_b32_e32 v62, 0
	s_waitcnt lgkmcnt(0)
	s_barrier
	s_waitcnt vmcnt(0)
	s_branch .LBB0_74

.LBB0_78:
	s_or_b64 exec, exec, s[0:1]
	v_readfirstlane_b32 s0, v63
	s_lshl_b32 s1, s0, 2
	s_and_b32 s1, s1, 60
	s_ashr_i32 s24, s0, 4
	s_add_i32 s24, s24, s1
	s_add_i32 s24, s24, 1
	s_cmp_lt_i32 s0, 48
	s_cselect_b32 s25, s24, -1
	s_mov_b32 s26, s36
	s_mov_b32 s27, s35
	s_mov_b32 s38, 0
	s_mov_b32 s39, 0
	s_cmp_lt_i32 s25, 0
	s_cbranch_scc1 .Lrl_last
	s_lshl_b32 s0, s25, 5
	s_add_i32 s1, s0, 0x14400
	v_mov_b32_e32 v64, s1
	ds_read_b128 v[118:121], v64
	ds_read_b32 v122, v64 offset:16
	v_add_u32_e32 v65, s0, v111
	ds_read2_b32 v[124:125], v65 offset1:4
	s_lshl_b32 s0, s25, 8
	v_add_u32_e32 v63, s0, v113
	ds_read_b128 v[86:89], v63
	ds_read_b128 v[90:93], v63 offset:16
	ds_read_b128 v[94:97], v63 offset:32
	ds_read_b128 v[98:101], v63 offset:48
	s_waitcnt lgkmcnt(0)
	v_readfirstlane_b32 s27, v118
	v_readfirstlane_b32 s26, v119
	v_cndmask_b32_e64 v64, v122, v121, s[12:13]
	v_cndmask_b32_e64 v64, v64, v120, s[14:15]
	v_lshl_or_b32 v64, v64, 8, v107
	v_mov_b32_e32 v65, v62
	v_lshl_add_u64 v[64:65], v[0:1], 0, v[64:65]
	v_lshl_or_b32 v63, v124, 8, v107
	v_lshl_or_b32 v85, v125, 8, v107
	s_lshr_b32 s38, s27, 2
	s_and_b32 s39, s27, 3
	s_lshl_b32 s39, s39, 4
	s_branch .Lrl_go

.Lrl_go:
	s_add_i32 s1, s35, 3
	s_lshr_b32 s1, s1, 2
	s_waitcnt vmcnt(18)
	ds_bpermute_b32 v118, v108, v2
	ds_bpermute_b32 v115, v108, v3
	ds_bpermute_b32 v114, v108, v4
	ds_bpermute_b32 v127, v108, v5
	ds_bpermute_b32 v124, v109, v2
	ds_bpermute_b32 v126, v109, v3
	ds_bpermute_b32 v125, v109, v4
	ds_bpermute_b32 v123, v109, v5
	ds_bpermute_b32 v120, v110, v2
	ds_bpermute_b32 v122, v110, v3
	ds_bpermute_b32 v121, v110, v4
	ds_bpermute_b32 v119, v110, v5
	s_cmp_lt_i32 s25, 0
	s_cbranch_scc1 .Lrl_s1
	v_mov_b64_e32 v[2:3], 0
	v_mov_b64_e32 v[4:5], 0
	s_and_saveexec_b64 s[0:1], s[16:17]
	global_load_dwordx4 v[2:5], v[64:65], off sc0 nt
	s_or_b64 exec, exec, s[0:1]
.Lrl_s1:
	s_waitcnt vmcnt(18)
	v_mov_b64_e32 v[102:103], 0
	v_mov_b64_e32 v[104:105], 0
	s_cmp_gt_i32 s36, 0
	s_cbranch_scc0 .Lrl_c0a
	v_mov_b64_e32 v[102:103], v[6:7]
	v_mov_b64_e32 v[104:105], v[8:9]
.Lrl_c0a:
	s_cmp_lt_i32 s25, 0
	s_cbranch_scc1 .Lrl_s2
	s_cmp_gt_i32 s26, 0
	s_cbranch_scc0 .Lrl_c0d
	v_mov_b64_e32 v[6:7], 0
	v_mov_b64_e32 v[8:9], 0
	v_cmp_gt_i32_e32 vcc, s26, v106
	s_and_saveexec_b64 s[0:1], vcc
	global_load_dwordx4 v[6:9], v63, s[18:19] sc1
	s_or_b64 exec, exec, s[0:1]
	s_branch .Lrl_s2
.Lrl_c0d:
	global_load_dword v6, v62, s[18:19]
.Lrl_s2:
	s_waitcnt vmcnt(18)
	s_cmp_gt_i32 s36, 4
	s_cbranch_scc0 .Lrl_c1a
	v_pk_add_f32 v[102:103], v[102:103], v[10:11]
	v_pk_add_f32 v[104:105], v[104:105], v[12:13]
.Lrl_c1a:
	s_cmp_lt_i32 s25, 0
	s_cbranch_scc1 .Lrl_t0
	s_cmp_gt_i32 s26, 4
	s_cbranch_scc0 .Lrl_c1d
	v_mov_b64_e32 v[10:11], 0
	v_mov_b64_e32 v[12:13], 0
	v_cmp_gt_i32_e32 vcc, s26, v112
	s_and_saveexec_b64 s[0:1], vcc
	global_load_dwordx4 v[10:13], v85, s[18:19] sc1
	s_or_b64 exec, exec, s[0:1]
	s_branch .Lrl_t0
.Lrl_c1d:
	global_load_dword v10, v62, s[18:19]
.Lrl_t0:
	s_add_i32 s89, s35, 3
	s_lshr_b32 s89, s89, 2
	s_waitcnt vmcnt(18)
	v_mov_b64_e32 v[82:83], v[14:15]
	v_mov_b64_e32 v[84:85], v[16:17]
	s_cmp_gt_u32 s38, 0
	s_cbranch_scc0 .Lrl_p0
	v_lshl_or_b32 v63, v86, 8, v107
	global_load_dwordx4 v[14:17], v63, s[28:29] sc0 nt
.Lrl_c0:
	s_waitcnt vmcnt(18)
	s_cmp_lt_u32 s89, 2
	s_cbranch_scc1 .Lrl_a1
	v_pk_add_f32 v[82:83], v[82:83], v[18:19]
	v_pk_add_f32 v[84:85], v[84:85], v[20:21]
.Lrl_a1:
	s_cmp_gt_u32 s38, 1
	s_cbranch_scc0 .Lrl_p1
	v_lshl_or_b32 v63, v87, 8, v107
	global_load_dwordx4 v[18:21], v63, s[28:29] sc0 nt
.Lrl_c1:
	s_waitcnt vmcnt(18)
	s_cmp_lt_u32 s89, 3
	s_cbranch_scc1 .Lrl_a2
	v_pk_add_f32 v[82:83], v[82:83], v[22:23]
	v_pk_add_f32 v[84:85], v[84:85], v[24:25]
.Lrl_a2:
	s_cmp_gt_u32 s38, 2
	s_cbranch_scc0 .Lrl_p2
	v_lshl_or_b32 v63, v88, 8, v107
	global_load_dwordx4 v[22:25], v63, s[28:29] sc0 nt
.Lrl_c2:
	s_waitcnt vmcnt(18)
	s_cmp_lt_u32 s89, 4
	s_cbranch_scc1 .Lrl_a3
	v_pk_add_f32 v[82:83], v[82:83], v[26:27]
	v_pk_add_f32 v[84:85], v[84:85], v[28:29]
.Lrl_a3:
	s_cmp_gt_u32 s38, 3
	s_cbranch_scc0 .Lrl_p3
	v_lshl_or_b32 v63, v89, 8, v107
	global_load_dwordx4 v[26:29], v63, s[28:29] sc0 nt
.Lrl_c3:
	s_waitcnt vmcnt(18)
	s_cmp_lt_u32 s89, 5
	s_cbranch_scc1 .Lrl_a4
	v_pk_add_f32 v[82:83], v[82:83], v[30:31]
	v_pk_add_f32 v[84:85], v[84:85], v[32:33]
.Lrl_a4:
	s_cmp_gt_u32 s38, 4
	s_cbranch_scc0 .Lrl_p4
	v_lshl_or_b32 v63, v90, 8, v107
	global_load_dwordx4 v[30:33], v63, s[28:29] sc0 nt
.Lrl_c4:
	s_waitcnt vmcnt(18)
	s_cmp_lt_u32 s89, 6
	s_cbranch_scc1 .Lrl_a5
	v_pk_add_f32 v[82:83], v[82:83], v[34:35]
	v_pk_add_f32 v[84:85], v[84:85], v[36:37]
.Lrl_a5:
	s_cmp_gt_u32 s38, 5
	s_cbranch_scc0 .Lrl_p5
	v_lshl_or_b32 v63, v91, 8, v107
	global_load_dwordx4 v[34:37], v63, s[28:29] sc0 nt
.Lrl_c5:
	s_waitcnt vmcnt(18)
	s_cmp_lt_u32 s89, 7
	s_cbranch_scc1 .Lrl_a6
	v_pk_add_f32 v[82:83], v[82:83], v[38:39]
	v_pk_add_f32 v[84:85], v[84:85], v[40:41]
.Lrl_a6:
	s_cmp_gt_u32 s38, 6
	s_cbranch_scc0 .Lrl_p6
	v_lshl_or_b32 v63, v92, 8, v107
	global_load_dwordx4 v[38:41], v63, s[28:29] sc0 nt
.Lrl_c6:
	s_waitcnt vmcnt(18)
	s_cmp_lt_u32 s89, 8
	s_cbranch_scc1 .Lrl_a7
	v_pk_add_f32 v[82:83], v[82:83], v[42:43]
	v_pk_add_f32 v[84:85], v[84:85], v[44:45]
.Lrl_a7:
	s_cmp_gt_u32 s38, 7
	s_cbranch_scc0 .Lrl_p7
	v_lshl_or_b32 v63, v93, 8, v107
	global_load_dwordx4 v[42:45], v63, s[28:29] sc0 nt
.Lrl_c7:
	s_waitcnt vmcnt(18)
	s_cmp_lt_u32 s89, 9
	s_cbranch_scc1 .Lrl_a8
	v_pk_add_f32 v[82:83], v[82:83], v[46:47]
	v_pk_add_f32 v[84:85], v[84:85], v[48:49]
.Lrl_a8:
	s_cmp_gt_u32 s38, 8
	s_cbranch_scc0 .Lrl_p8
	v_lshl_or_b32 v63, v94, 8, v107
	global_load_dwordx4 v[46:49], v63, s[28:29] sc0 nt
.Lrl_c8:
	s_waitcnt vmcnt(18)
	s_cmp_lt_u32 s89, 10
	s_cbranch_scc1 .Lrl_a9
	v_pk_add_f32 v[82:83], v[82:83], v[50:51]
	v_pk_add_f32 v[84:85], v[84:85], v[52:53]
.Lrl_a9:
	s_cmp_gt_u32 s38, 9
	s_cbranch_scc0 .Lrl_p9
	v_lshl_or_b32 v63, v95, 8, v107
	global_load_dwordx4 v[50:53], v63, s[28:29] sc0 nt
.Lrl_c9:
	s_waitcnt vmcnt(18)
	s_cmp_lt_u32 s89, 11
	s_cbranch_scc1 .Lrl_a10
	v_pk_add_f32 v[82:83], v[82:83], v[54:55]
	v_pk_add_f32 v[84:85], v[84:85], v[56:57]
.Lrl_a10:
	s_cmp_gt_u32 s38, 10
	s_cbranch_scc0 .Lrl_p10
	v_lshl_or_b32 v63, v96, 8, v107
	global_load_dwordx4 v[54:57], v63, s[28:29] sc0 nt
.Lrl_c10:
	s_waitcnt vmcnt(18)
	s_cmp_lt_u32 s89, 12
	s_cbranch_scc1 .Lrl_a11
	v_pk_add_f32 v[82:83], v[82:83], v[58:59]
	v_pk_add_f32 v[84:85], v[84:85], v[60:61]
.Lrl_a11:
	s_cmp_gt_u32 s38, 11
	s_cbranch_scc0 .Lrl_p11
	v_lshl_or_b32 v63, v97, 8, v107
	global_load_dwordx4 v[58:61], v63, s[28:29] sc0 nt
.Lrl_c11:
	s_waitcnt vmcnt(18)
	s_cmp_lt_u32 s89, 13
	s_cbranch_scc1 .Lrl_a12
	v_pk_add_f32 v[82:83], v[82:83], v[66:67]
	v_pk_add_f32 v[84:85], v[84:85], v[68:69]
.Lrl_a12:
	s_cmp_gt_u32 s38, 12
	s_cbranch_scc0 .Lrl_p12
	v_lshl_or_b32 v63, v98, 8, v107
	global_load_dwordx4 v[66:69], v63, s[28:29] sc0 nt
.Lrl_c12:
	s_waitcnt vmcnt(18)
	s_cmp_lt_u32 s89, 14
	s_cbranch_scc1 .Lrl_a13
	v_pk_add_f32 v[82:83], v[82:83], v[70:71]
	v_pk_add_f32 v[84:85], v[84:85], v[72:73]
.Lrl_a13:
	s_cmp_gt_u32 s38, 13
	s_cbranch_scc0 .Lrl_p13
	v_lshl_or_b32 v63, v99, 8, v107
	global_load_dwordx4 v[70:73], v63, s[28:29] sc0 nt
.Lrl_c13:
	s_waitcnt vmcnt(18)
	s_cmp_lt_u32 s89, 15
	s_cbranch_scc1 .Lrl_a14
	v_pk_add_f32 v[82:83], v[82:83], v[74:75]
	v_pk_add_f32 v[84:85], v[84:85], v[76:77]
.Lrl_a14:
	s_cmp_gt_u32 s38, 14
	s_cbranch_scc0 .Lrl_p14
	v_lshl_or_b32 v63, v100, 8, v107
	global_load_dwordx4 v[74:77], v63, s[28:29] sc0 nt
.Lrl_c14:
	s_waitcnt vmcnt(18)
	s_cmp_lt_u32 s89, 16
	s_cbranch_scc1 .Lrl_a15
	v_pk_add_f32 v[82:83], v[82:83], v[78:79]
	v_pk_add_f32 v[84:85], v[84:85], v[80:81]
.Lrl_a15:
	s_cmp_gt_u32 s38, 15
	s_cbranch_scc0 .Lrl_p15
	v_lshl_or_b32 v63, v101, 8, v107
	global_load_dwordx4 v[78:81], v63, s[28:29] sc0 nt

.Lrl_p0:
	s_cmp_lt_i32 s25, 0
	s_cbranch_scc1 .Lrl_c0
	s_cmp_eq_u32 s38, 0
	s_cbranch_scc0 .Lrl_d0
	s_cmp_eq_u32 s39, 0
	s_cbranch_scc1 .Lrl_d0
	v_lshl_or_b32 v63, v86, 8, v107
	v_mov_b64_e32 v[14:15], 0
	v_mov_b64_e32 v[16:17], 0
	s_mov_b64 s[0:1], exec
	s_bfm_b64 exec, s39, 0
	global_load_dwordx4 v[14:17], v63, s[28:29] sc0 nt
	s_mov_b64 exec, s[0:1]
	s_branch .Lrl_c0
.Lrl_d0:
	global_load_dword v14, v62, s[18:19]
	s_branch .Lrl_c0
.Lrl_p1:
	s_cmp_lt_i32 s25, 0
	s_cbranch_scc1 .Lrl_c1
	s_cmp_eq_u32 s38, 1
	s_cbranch_scc0 .Lrl_d1
	s_cmp_eq_u32 s39, 0
	s_cbranch_scc1 .Lrl_d1
	v_lshl_or_b32 v63, v87, 8, v107
	v_mov_b64_e32 v[18:19], 0
	v_mov_b64_e32 v[20:21], 0
	s_mov_b64 s[0:1], exec
	s_bfm_b64 exec, s39, 0
	global_load_dwordx4 v[18:21], v63, s[28:29] sc0 nt
	s_mov_b64 exec, s[0:1]
	s_branch .Lrl_c1
.Lrl_d1:
	global_load_dword v18, v62, s[18:19]
	s_branch .Lrl_c1
.Lrl_p2:
	s_cmp_lt_i32 s25, 0
	s_cbranch_scc1 .Lrl_c2
	s_cmp_eq_u32 s38, 2
	s_cbranch_scc0 .Lrl_d2
	s_cmp_eq_u32 s39, 0
	s_cbranch_scc1 .Lrl_d2
	v_lshl_or_b32 v63, v88, 8, v107
	v_mov_b64_e32 v[22:23], 0
	v_mov_b64_e32 v[24:25], 0
	s_mov_b64 s[0:1], exec
	s_bfm_b64 exec, s39, 0
	global_load_dwordx4 v[22:25], v63, s[28:29] sc0 nt
	s_mov_b64 exec, s[0:1]
	s_branch .Lrl_c2
.Lrl_d2:
	global_load_dword v22, v62, s[18:19]
	s_branch .Lrl_c2
.Lrl_p3:
	s_cmp_lt_i32 s25, 0
	s_cbranch_scc1 .Lrl_c3
	s_cmp_eq_u32 s38, 3
	s_cbranch_scc0 .Lrl_d3
	s_cmp_eq_u32 s39, 0
	s_cbranch_scc1 .Lrl_d3
	v_lshl_or_b32 v63, v89, 8, v107
	v_mov_b64_e32 v[26:27], 0
	v_mov_b64_e32 v[28:29], 0
	s_mov_b64 s[0:1], exec
	s_bfm_b64 exec, s39, 0
	global_load_dwordx4 v[26:29], v63, s[28:29] sc0 nt
	s_mov_b64 exec, s[0:1]
	s_branch .Lrl_c3
.Lrl_d3:
	global_load_dword v26, v62, s[18:19]
	s_branch .Lrl_c3
.Lrl_p4:
	s_cmp_lt_i32 s25, 0
	s_cbranch_scc1 .Lrl_c4
	s_cmp_eq_u32 s38, 4
	s_cbranch_scc0 .Lrl_d4
	s_cmp_eq_u32 s39, 0
	s_cbranch_scc1 .Lrl_d4
	v_lshl_or_b32 v63, v90, 8, v107
	v_mov_b64_e32 v[30:31], 0
	v_mov_b64_e32 v[32:33], 0
	s_mov_b64 s[0:1], exec
	s_bfm_b64 exec, s39, 0
	global_load_dwordx4 v[30:33], v63, s[28:29] sc0 nt
	s_mov_b64 exec, s[0:1]
	s_branch .Lrl_c4
.Lrl_d4:
	global_load_dword v30, v62, s[18:19]
	s_branch .Lrl_c4
.Lrl_p5:
	s_cmp_lt_i32 s25, 0
	s_cbranch_scc1 .Lrl_c5
	s_cmp_eq_u32 s38, 5
	s_cbranch_scc0 .Lrl_d5
	s_cmp_eq_u32 s39, 0
	s_cbranch_scc1 .Lrl_d5
	v_lshl_or_b32 v63, v91, 8, v107
	v_mov_b64_e32 v[34:35], 0
	v_mov_b64_e32 v[36:37], 0
	s_mov_b64 s[0:1], exec
	s_bfm_b64 exec, s39, 0
	global_load_dwordx4 v[34:37], v63, s[28:29] sc0 nt
	s_mov_b64 exec, s[0:1]
	s_branch .Lrl_c5
.Lrl_d5:
	global_load_dword v34, v62, s[18:19]
	s_branch .Lrl_c5
.Lrl_p6:
	s_cmp_lt_i32 s25, 0
	s_cbranch_scc1 .Lrl_c6
	s_cmp_eq_u32 s38, 6
	s_cbranch_scc0 .Lrl_d6
	s_cmp_eq_u32 s39, 0
	s_cbranch_scc1 .Lrl_d6
	v_lshl_or_b32 v63, v92, 8, v107
	v_mov_b64_e32 v[38:39], 0
	v_mov_b64_e32 v[40:41], 0
	s_mov_b64 s[0:1], exec
	s_bfm_b64 exec, s39, 0
	global_load_dwordx4 v[38:41], v63, s[28:29] sc0 nt
	s_mov_b64 exec, s[0:1]
	s_branch .Lrl_c6
.Lrl_d6:
	global_load_dword v38, v62, s[18:19]
	s_branch .Lrl_c6
.Lrl_p7:
	s_cmp_lt_i32 s25, 0
	s_cbranch_scc1 .Lrl_c7
	s_cmp_eq_u32 s38, 7
	s_cbranch_scc0 .Lrl_d7
	s_cmp_eq_u32 s39, 0
	s_cbranch_scc1 .Lrl_d7
	v_lshl_or_b32 v63, v93, 8, v107
	v_mov_b64_e32 v[42:43], 0
	v_mov_b64_e32 v[44:45], 0
	s_mov_b64 s[0:1], exec
	s_bfm_b64 exec, s39, 0
	global_load_dwordx4 v[42:45], v63, s[28:29] sc0 nt
	s_mov_b64 exec, s[0:1]
	s_branch .Lrl_c7
.Lrl_d7:
	global_load_dword v42, v62, s[18:19]
	s_branch .Lrl_c7
.Lrl_p8:
	s_cmp_lt_i32 s25, 0
	s_cbranch_scc1 .Lrl_c8
	s_cmp_eq_u32 s38, 8
	s_cbranch_scc0 .Lrl_d8
	s_cmp_eq_u32 s39, 0
	s_cbranch_scc1 .Lrl_d8
	v_lshl_or_b32 v63, v94, 8, v107
	v_mov_b64_e32 v[46:47], 0
	v_mov_b64_e32 v[48:49], 0
	s_mov_b64 s[0:1], exec
	s_bfm_b64 exec, s39, 0
	global_load_dwordx4 v[46:49], v63, s[28:29] sc0 nt
	s_mov_b64 exec, s[0:1]
	s_branch .Lrl_c8
.Lrl_d8:
	global_load_dword v46, v62, s[18:19]
	s_branch .Lrl_c8
.Lrl_p9:
	s_cmp_lt_i32 s25, 0
	s_cbranch_scc1 .Lrl_c9
	s_cmp_eq_u32 s38, 9
	s_cbranch_scc0 .Lrl_d9
	s_cmp_eq_u32 s39, 0
	s_cbranch_scc1 .Lrl_d9
	v_lshl_or_b32 v63, v95, 8, v107
	v_mov_b64_e32 v[50:51], 0
	v_mov_b64_e32 v[52:53], 0
	s_mov_b64 s[0:1], exec
	s_bfm_b64 exec, s39, 0
	global_load_dwordx4 v[50:53], v63, s[28:29] sc0 nt
	s_mov_b64 exec, s[0:1]
	s_branch .Lrl_c9
.Lrl_d9:
	global_load_dword v50, v62, s[18:19]
	s_branch .Lrl_c9
.Lrl_p10:
	s_cmp_lt_i32 s25, 0
	s_cbranch_scc1 .Lrl_c10
	s_cmp_eq_u32 s38, 10
	s_cbranch_scc0 .Lrl_d10
	s_cmp_eq_u32 s39, 0
	s_cbranch_scc1 .Lrl_d10
	v_lshl_or_b32 v63, v96, 8, v107
	v_mov_b64_e32 v[54:55], 0
	v_mov_b64_e32 v[56:57], 0
	s_mov_b64 s[0:1], exec
	s_bfm_b64 exec, s39, 0
	global_load_dwordx4 v[54:57], v63, s[28:29] sc0 nt
	s_mov_b64 exec, s[0:1]
	s_branch .Lrl_c10
.Lrl_d10:
	global_load_dword v54, v62, s[18:19]
	s_branch .Lrl_c10
.Lrl_p11:
	s_cmp_lt_i32 s25, 0
	s_cbranch_scc1 .Lrl_c11
	s_cmp_eq_u32 s38, 11
	s_cbranch_scc0 .Lrl_d11
	s_cmp_eq_u32 s39, 0
	s_cbranch_scc1 .Lrl_d11
	v_lshl_or_b32 v63, v97, 8, v107
	v_mov_b64_e32 v[58:59], 0
	v_mov_b64_e32 v[60:61], 0
	s_mov_b64 s[0:1], exec
	s_bfm_b64 exec, s39, 0
	global_load_dwordx4 v[58:61], v63, s[28:29] sc0 nt
	s_mov_b64 exec, s[0:1]
	s_branch .Lrl_c11
.Lrl_d11:
	global_load_dword v58, v62, s[18:19]
	s_branch .Lrl_c11
.Lrl_p12:
	s_cmp_lt_i32 s25, 0
	s_cbranch_scc1 .Lrl_c12
	s_cmp_eq_u32 s38, 12
	s_cbranch_scc0 .Lrl_d12
	s_cmp_eq_u32 s39, 0
	s_cbranch_scc1 .Lrl_d12
	v_lshl_or_b32 v63, v98, 8, v107
	v_mov_b64_e32 v[66:67], 0
	v_mov_b64_e32 v[68:69], 0
	s_mov_b64 s[0:1], exec
	s_bfm_b64 exec, s39, 0
	global_load_dwordx4 v[66:69], v63, s[28:29] sc0 nt
	s_mov_b64 exec, s[0:1]
	s_branch .Lrl_c12
.Lrl_d12:
	global_load_dword v66, v62, s[18:19]
	s_branch .Lrl_c12
.Lrl_p13:
	s_cmp_lt_i32 s25, 0
	s_cbranch_scc1 .Lrl_c13
	s_cmp_eq_u32 s38, 13
	s_cbranch_scc0 .Lrl_d13
	s_cmp_eq_u32 s39, 0
	s_cbranch_scc1 .Lrl_d13
	v_lshl_or_b32 v63, v99, 8, v107
	v_mov_b64_e32 v[70:71], 0
	v_mov_b64_e32 v[72:73], 0
	s_mov_b64 s[0:1], exec
	s_bfm_b64 exec, s39, 0
	global_load_dwordx4 v[70:73], v63, s[28:29] sc0 nt
	s_mov_b64 exec, s[0:1]
	s_branch .Lrl_c13
.Lrl_d13:
	global_load_dword v70, v62, s[18:19]
	s_branch .Lrl_c13
.Lrl_p14:
	s_cmp_lt_i32 s25, 0
	s_cbranch_scc1 .Lrl_c14
	s_cmp_eq_u32 s38, 14
	s_cbranch_scc0 .Lrl_d14
	s_cmp_eq_u32 s39, 0
	s_cbranch_scc1 .Lrl_d14
	v_lshl_or_b32 v63, v100, 8, v107
	v_mov_b64_e32 v[74:75], 0
	v_mov_b64_e32 v[76:77], 0
	s_mov_b64 s[0:1], exec
	s_bfm_b64 exec, s39, 0
	global_load_dwordx4 v[74:77], v63, s[28:29] sc0 nt
	s_mov_b64 exec, s[0:1]
	s_branch .Lrl_c14
.Lrl_d14:
	global_load_dword v74, v62, s[18:19]
	s_branch .Lrl_c14
.Lrl_p15:
	s_cmp_lt_i32 s25, 0
	s_cbranch_scc1 .Lrl_c15
	s_cmp_eq_u32 s38, 15
	s_cbranch_scc0 .Lrl_d15
	s_cmp_eq_u32 s39, 0
	s_cbranch_scc1 .Lrl_d15
	v_lshl_or_b32 v63, v101, 8, v107
	v_mov_b64_e32 v[78:79], 0
	v_mov_b64_e32 v[80:81], 0
	s_mov_b64 s[0:1], exec
	s_bfm_b64 exec, s39, 0
	global_load_dwordx4 v[78:81], v63, s[28:29] sc0 nt
	s_mov_b64 exec, s[0:1]
	s_branch .Lrl_c15
.Lrl_d15:
	global_load_dword v78, v62, s[18:19]
	s_branch .Lrl_c15
